# also touch the code object's kernel descriptors from each kernel
# baseline (speedup 1.0000x reference)
.LBB0_6:
	s_or_b64 exec, exec, s[4:5]
	s_waitcnt lgkmcnt(0)
	s_barrier
	ds_read_b32 v19, v29
	v_lshl_add_u32 v26, v26, s8, v27
	ds_read_b32 v27, v30
	ds_read_b32 v28, v28
	ds_read_b32 v25, v25
	s_waitcnt vmcnt(3)
	v_cmp_eq_u32_e32 vcc, 0, v17
	s_mov_b64 s[4:5], -1
	s_waitcnt lgkmcnt(3)
	v_add_lshl_u32 v19, v26, v19, 2
	ds_write2st64_b32 v19, v8, v9 offset1:64
	v_bfrev_b32_e32 v8, 1
	v_cndmask_b32_e32 v8, 0, v8, vcc
	v_or_b32_e32 v8, v8, v0
	ds_write_b32 v19, v8 offset:32768
	v_lshl_add_u32 v8, v20, s8, v21
	s_waitcnt lgkmcnt(4)
	v_add_lshl_u32 v8, v8, v27, 2
	ds_write2st64_b32 v8, v4, v5 offset1:64
	v_mov_b32_e32 v4, 0x400
	v_mov_b32_e32 v5, 0x80000400
	s_waitcnt vmcnt(2)
	v_cmp_eq_u32_e32 vcc, 0, v16
	s_nop 1
	v_cndmask_b32_e32 v4, v4, v5, vcc
	v_or_b32_e32 v4, v4, v0
	ds_write_b32 v8, v4 offset:32768
	v_lshl_add_u32 v4, v22, s8, v23
	s_waitcnt lgkmcnt(5)
	v_add_lshl_u32 v4, v4, v28, 2
	ds_write2st64_b32 v4, v6, v7 offset1:64
	v_mov_b32_e32 v5, 0x800
	v_mov_b32_e32 v6, 0x80000800
	s_waitcnt vmcnt(1)
	v_cmp_eq_u32_e32 vcc, 0, v15
	s_nop 1
	v_cndmask_b32_e32 v5, v5, v6, vcc
	v_or_b32_e32 v5, v5, v0
	ds_write_b32 v4, v5 offset:32768
	v_lshl_add_u32 v4, v24, s8, v18
	s_waitcnt lgkmcnt(6)
	v_add_lshl_u32 v4, v4, v25, 2
	ds_write2st64_b32 v4, v2, v3 offset1:64
	v_mov_b32_e32 v2, 0xc00
	v_mov_b32_e32 v3, 0x80000c00
	s_waitcnt vmcnt(0)
	v_cmp_eq_u32_e32 vcc, 0, v14
	s_nop 1
	v_cndmask_b32_e32 v2, v2, v3, vcc
	v_or_b32_e32 v2, v2, v0
	ds_write_b32 v4, v2 offset:32768
	s_waitcnt lgkmcnt(0)
	s_barrier
	s_getpc_b64 s[30:31]
	s_add_u32 s30, s30, 0x24b8
	s_addc_u32 s31, s31, 0
	v_lshlrev_b32_e32 v40, 6, v0
	v_min_u32_e32 v40, 0x2d00, v40
	global_load_dword v40, v40, s[30:31]
	s_and_b32 s32, s0, 0xfffff000
	s_mov_b32 s33, s1
	v_and_b32_e32 v41, 63, v0
	v_lshlrev_b32_e32 v41, 6, v41
	global_load_dword v41, v41, s[32:33]
	s_sub_u32 s34, s30, 0x3c80
	s_subb_u32 s35, s31, 0
	v_and_b32_e32 v42, 63, v0
	v_lshlrev_b32_e32 v42, 6, v42
	v_min_u32_e32 v42, 0x140, v42
	global_load_dword v42, v42, s[34:35]
	ds_read_b32 v14, v11 offset:32768
	s_mov_b64 s[18:19], s[44:45]
	s_mov_b64 s[8:9], s[36:37]
	s_mov_b64 s[10:11], s[38:39]
	s_mov_b64 s[12:13], s[40:41]
	s_mov_b64 s[14:15], s[42:43]
	ds_read2st64_b32 v[4:5], v11 offset1:64
	v_or_b32_e32 v2, s16, v0
	v_mov_b32_e32 v3, 0
	s_waitcnt lgkmcnt(0)
	v_and_b32_e32 v15, 0x7fffffff, v14
	s_and_b64 vcc, exec, s[2:3]
	v_lshlrev_b64 v[6:7], 2, v[2:3]
	s_cbranch_vccz .LBB0_8
	v_lshl_add_u64 v[8:9], s[10:11], 0, v[6:7]
	global_store_dword v[8:9], v4, off
	v_lshl_add_u64 v[8:9], s[12:13], 0, v[6:7]
	global_store_dword v[8:9], v5, off
	v_lshl_add_u64 v[8:9], s[14:15], 0, v[6:7]
	global_store_dword v[8:9], v15, off
	s_mov_b64 s[4:5], 0

.Lfirst_pc:
	s_add_u32 s66, s66, (.Lfirst_code_end-.Lfirst_pc)&4294967295
	s_addc_u32 s67, s67, 0
	s_lshl_b32 s68, s27, 12
	v_lshl_or_b32 v214, v44, 6, s68
	v_min_u32_e32 v214, 0x3300, v214
	global_load_dword v214, v214, s[66:67]
	v_lshlrev_b32_e32 v215, 6, v44
	global_load_dword v215, v215, s[96:97]
	s_sub_u32 s68, s66, 0x6b80
	s_subb_u32 s69, s67, 0
	v_lshlrev_b32_e32 v209, 6, v44
	v_min_u32_e32 v209, 0x140, v209
	global_load_dword v209, v209, s[68:69]
	s_andn2_b64 vcc, exec, s[0:1]
	s_waitcnt lgkmcnt(0)
	s_barrier
	s_cbranch_vccnz .LBB2_117
	v_lshlrev_b32_e32 v0, 3, v1
	v_add_u32_e32 v0, 0x7000, v0
	ds_read2_b64 v[12:15], v0 offset0:196 offset1:198
	ds_read2_b64 v[8:11], v0 offset0:200 offset1:202
	ds_read2_b64 v[4:7], v0 offset0:204 offset1:206
	ds_read2_b64 v[0:3], v0 offset0:208 offset1:210
	v_mov_b32_e32 v21, 0
	ds_read_b32 v36, v21 offset:30368
	s_cmp_lt_i32 s39, 4
	s_mov_b64 s[0:1], 0
	s_cbranch_scc1 .LBB2_118
	s_cmp_gt_i32 s39, 4
	s_cbranch_scc0 .LBB2_119
	s_cmp_gt_i32 s39, 5
	s_cbranch_scc0 .LBB2_129
	s_mov_b64 s[8:9], 0
	s_cmp_eq_u32 s39, 6
	s_mov_b64 s[14:15], 0
	s_cbranch_scc0 .LBB2_107
	v_mov_b32_e32 v37, 0
	s_waitcnt lgkmcnt(4)
	v_dot2c_f32_f16_e32 v37, v20, v12
	v_mov_b32_e32 v20, 0
	v_dot2c_f32_f16_e32 v20, v49, v13
	v_dot2c_f32_f16_e32 v37, v54, v14
	v_dot2c_f32_f16_e32 v20, v57, v15
	s_waitcnt lgkmcnt(3)
	v_dot2c_f32_f16_e32 v37, v61, v8
	v_dot2c_f32_f16_e32 v20, v64, v9
	v_dot2c_f32_f16_e32 v37, v67, v10
	v_dot2c_f32_f16_e32 v20, v69, v11
	s_waitcnt lgkmcnt(2)
	v_dot2c_f32_f16_e32 v37, v75, v4
	v_dot2c_f32_f16_e32 v20, v79, v5
	v_dot2c_f32_f16_e32 v37, v85, v6
	v_dot2c_f32_f16_e32 v20, v88, v7
	s_waitcnt lgkmcnt(1)
	v_dot2c_f32_f16_e32 v37, v91, v0
	v_dot2c_f32_f16_e32 v20, v94, v1
	v_dot2c_f32_f16_e32 v37, v97, v2
	v_dot2c_f32_f16_e32 v20, v98, v3
	s_and_b64 vcc, s[18:19], s[12:13]
	v_cndmask_b32_e32 v35, -1, v35, vcc
	v_mov_b32_e32 v21, 0
	v_add_f32_e32 v20, v37, v20
	v_mov_b32_e32 v37, v20
	s_nop 1
	v_permlane32_swap_b32_e32 v20, v37
	v_cmp_lt_i32_e32 vcc, -1, v35
	s_and_saveexec_b64 s[12:13], vcc
	s_cbranch_execz .LBB2_106
	v_add_f32_e32 v20, v20, v37
	s_waitcnt lgkmcnt(0)
	v_mul_f32_e32 v37, v36, v20
	v_add_u32_e32 v20, s58, v35
	v_lshl_add_u64 v[20:21], v[20:21], 2, s[34:35]
	global_atomic_add_f32 v[20:21], v37, off

.Lff_pc:
	s_add_u32 s36, s36, (.Lff_code_end-.Lff_pc)&4294967295
	s_addc_u32 s37, s37, 0
	v_lshlrev_b32_e32 v183, 6, v0
	v_min_u32_e32 v183, 0x3300, v183
	global_load_dword v183, v183, s[36:37]
	v_lshlrev_b32_e32 v182, 6, v38
	global_load_dword v182, v182, s[38:39]
	s_sub_u32 s40, s36, 0x9f80
	s_subb_u32 s41, s37, 0
	v_lshlrev_b32_e32 v181, 6, v38
	v_min_u32_e32 v181, 0x140, v181
	global_load_dword v181, v181, s[40:41]
	s_mov_b32 s4, 0x42c80000
	v_cndmask_b32_e32 v3, 0, v3, vcc
	v_cmp_lt_f32_e32 vcc, 0, v131
	v_cmp_ngt_f32_e64 s[2:3], s4, v3
	s_mov_b64 s[6:7], 0
	v_cndmask_b32_e32 v4, 0, v4, vcc
	v_cmp_lt_f32_e32 vcc, 0, v130
	s_nop 1
	v_cndmask_b32_e32 v5, 0, v5, vcc
	v_cmp_lt_f32_e32 vcc, 0, v129
	s_nop 1
	v_cndmask_b32_e32 v6, 0, v6, vcc
	v_cmp_lt_f32_e32 vcc, 0, v128
	s_nop 1
	v_cndmask_b32_e32 v7, 0, v7, vcc
	v_cmp_ngt_f32_e32 vcc, s4, v2
	s_or_b64 s[2:3], vcc, s[2:3]
	v_cmp_ngt_f32_e32 vcc, s4, v4
	s_or_b64 s[2:3], s[2:3], vcc
	v_cmp_ngt_f32_e32 vcc, s4, v5
	s_or_b64 s[2:3], s[2:3], vcc
	v_cmp_ngt_f32_e32 vcc, s4, v6
	s_or_b64 s[2:3], s[2:3], vcc
	v_cmp_ngt_f32_e32 vcc, s4, v7
	s_or_b64 s[2:3], s[2:3], vcc
	v_cndmask_b32_e64 v8, 0, 1, s[2:3]
	v_cmp_ne_u32_e32 vcc, 0, v8
	s_cmp_eq_u64 vcc, 0
	s_cselect_b64 s[2:3], -1, 0
	v_cndmask_b32_e64 v8, 0, 1, s[2:3]
	s_nop 0
	v_readfirstlane_b32 s2, v8
	s_bitcmp0_b32 s2, 0
	s_cbranch_scc0 .LBB3_45
	s_cmp_lt_i32 s26, 4
	s_cbranch_scc1 .LBB3_46
	s_cmp_gt_i32 s26, 4
	s_cbranch_scc0 .LBB3_47
	s_mov_b64 s[4:5], -1
	v_mov_b32_e32 v8, 0
	s_cmp_gt_i32 s26, 5
	v_mov_b32_e32 v167, 0
	v_mov_b32_e32 v166, 0
	v_mov_b32_e32 v165, 0
	v_mov_b32_e32 v164, 0
	v_mov_b32_e32 v162, 0
	v_mov_b32_e32 v160, 0
	v_mov_b32_e32 v159, 0
	v_mov_b32_e32 v157, 0
	v_mov_b32_e32 v151, 0
	v_mov_b32_e32 v149, 0
	v_mov_b32_e32 v147, 0
	v_mov_b32_e32 v146, 0
	v_mov_b32_e32 v144, 0
	v_mov_b32_e32 v143, 0
	v_mov_b32_e32 v152, 0
	v_mov_b32_e32 v153, 0
	v_mov_b32_e32 v154, 0
	v_mov_b32_e32 v155, 0
	v_mov_b32_e32 v156, 0
	v_mov_b32_e32 v158, 0
	v_mov_b32_e32 v161, 0
	v_mov_b32_e32 v163, 0
	v_mov_b32_e32 v168, 0
	v_mov_b32_e32 v169, 0
	v_mov_b32_e32 v170, 0
	v_mov_b32_e32 v171, 0
	v_mov_b32_e32 v172, 0
	v_mov_b32_e32 v173, 0
	v_mov_b32_e32 v174, 0
	v_mov_b32_e32 v145, 0
	v_mov_b32_e32 v148, 0
	v_mov_b32_e32 v150, 0
	s_cbranch_scc0 .LBB3_50
	s_cmp_eq_u32 s26, 6
	s_cbranch_scc0 .LBB3_49
	v_mov_b32_e32 v145, 0
	v_mov_b32_e32 v148, 0
	v_mov_b32_e32 v150, 0
	v_mov_b32_e32 v143, 0
	v_mov_b32_e32 v144, 0
	v_mov_b32_e32 v146, 0
	v_mov_b32_e32 v147, 0
	v_mov_b32_e32 v149, 0
	v_mov_b32_e32 v151, 0
	v_mov_b32_e32 v152, 0
	v_mov_b32_e32 v153, 0
	v_mov_b32_e32 v154, 0
	v_mov_b32_e32 v155, 0
	v_mov_b32_e32 v156, 0
	v_mov_b32_e32 v158, 0
	v_mov_b32_e32 v161, 0
	v_mov_b32_e32 v163, 0
	v_mov_b32_e32 v157, 0
	v_mov_b32_e32 v159, 0
	v_mov_b32_e32 v160, 0
	v_mov_b32_e32 v162, 0
	v_mov_b32_e32 v164, 0
	v_mov_b32_e32 v165, 0
	v_mov_b32_e32 v166, 0
	v_mov_b32_e32 v167, 0
	v_mov_b32_e32 v168, 0
	v_mov_b32_e32 v169, 0
	v_mov_b32_e32 v170, 0
	v_mov_b32_e32 v171, 0
	v_mov_b32_e32 v172, 0
	v_mov_b32_e32 v173, 0
	v_mov_b32_e32 v174, 0
	v_fma_mix_f32 v148, v43, v7, v148 op_sel_hi:[1,0,0]
	v_fma_mix_f32 v150, v45, v7, v150 op_sel_hi:[1,0,0]
	v_fma_mix_f32 v143, v50, v7, v143 op_sel_hi:[1,0,0]
	v_fma_mix_f32 v144, v54, v7, v144 op_sel_hi:[1,0,0]
	v_fma_mix_f32 v146, v58, v7, v146 op_sel_hi:[1,0,0]
	v_fma_mix_f32 v147, v61, v7, v147 op_sel_hi:[1,0,0]
	v_fma_mix_f32 v149, v64, v7, v149 op_sel_hi:[1,0,0]
	v_fma_mix_f32 v151, v66, v7, v151 op_sel_hi:[1,0,0]
	v_fma_mix_f32 v152, v43, v7, v152 op_sel:[1,0,0] op_sel_hi:[1,0,0]
	v_fma_mix_f32 v153, v45, v7, v153 op_sel:[1,0,0] op_sel_hi:[1,0,0]
	v_fma_mix_f32 v154, v50, v7, v154 op_sel:[1,0,0] op_sel_hi:[1,0,0]
	v_fma_mix_f32 v155, v54, v7, v155 op_sel:[1,0,0] op_sel_hi:[1,0,0]
	v_fma_mix_f32 v156, v58, v7, v156 op_sel:[1,0,0] op_sel_hi:[1,0,0]
	v_fma_mix_f32 v158, v61, v7, v158 op_sel:[1,0,0] op_sel_hi:[1,0,0]
	v_fma_mix_f32 v161, v64, v7, v161 op_sel:[1,0,0] op_sel_hi:[1,0,0]
	v_fma_mix_f32 v163, v66, v7, v163 op_sel:[1,0,0] op_sel_hi:[1,0,0]
	v_fma_mix_f32 v157, v72, v7, v157 op_sel_hi:[1,0,0]
	v_fma_mix_f32 v159, v76, v7, v159 op_sel_hi:[1,0,0]
	v_fma_mix_f32 v160, v83, v7, v160 op_sel_hi:[1,0,0]
	v_fma_mix_f32 v162, v85, v7, v162 op_sel_hi:[1,0,0]
	v_fma_mix_f32 v164, v89, v7, v164 op_sel_hi:[1,0,0]
	v_fma_mix_f32 v165, v92, v7, v165 op_sel_hi:[1,0,0]
	v_fma_mix_f32 v166, v95, v7, v166 op_sel_hi:[1,0,0]
	v_fma_mix_f32 v167, v96, v7, v167 op_sel_hi:[1,0,0]
	v_fma_mix_f32 v168, v72, v7, v168 op_sel:[1,0,0] op_sel_hi:[1,0,0]
	v_fma_mix_f32 v169, v76, v7, v169 op_sel:[1,0,0] op_sel_hi:[1,0,0]
	v_fma_mix_f32 v170, v83, v7, v170 op_sel:[1,0,0] op_sel_hi:[1,0,0]
	v_fma_mix_f32 v171, v85, v7, v171 op_sel:[1,0,0] op_sel_hi:[1,0,0]
	v_fma_mix_f32 v172, v89, v7, v172 op_sel:[1,0,0] op_sel_hi:[1,0,0]
	v_fma_mix_f32 v173, v92, v7, v173 op_sel:[1,0,0] op_sel_hi:[1,0,0]
	v_fma_mix_f32 v174, v95, v7, v174 op_sel:[1,0,0] op_sel_hi:[1,0,0]
	v_fma_mix_f32 v145, v96, v7, v145 op_sel:[1,0,0] op_sel_hi:[1,0,0]
	s_branch .LBB3_50

	.amdhsa_kernel _Z6k_iterILb0ELb0EEvPKfS1_PKiPK15HIP_vector_typeIfLj4EES7_S1_S1_S3_S1_PfS8_S1_S3_PDF16_PS5_SA_PiSA_SB_
		.amdhsa_group_segment_fixed_size 5808
		.amdhsa_private_segment_fixed_size 0
		.amdhsa_kernarg_size 152
		.amdhsa_user_sgpr_count 2
		.amdhsa_user_sgpr_dispatch_ptr 0
		.amdhsa_user_sgpr_queue_ptr 0
		.amdhsa_user_sgpr_kernarg_segment_ptr 1
		.amdhsa_user_sgpr_dispatch_id 0
		.amdhsa_user_sgpr_kernarg_preload_length 0
		.amdhsa_user_sgpr_kernarg_preload_offset 0
		.amdhsa_user_sgpr_private_segment_size 0
		.amdhsa_uses_dynamic_stack 0
		.amdhsa_enable_private_segment 0
		.amdhsa_system_sgpr_workgroup_id_x 1
		.amdhsa_system_sgpr_workgroup_id_y 0
		.amdhsa_system_sgpr_workgroup_id_z 0
		.amdhsa_system_sgpr_workgroup_info 0
		.amdhsa_system_vgpr_workitem_id 0
		.amdhsa_next_free_vgpr 184
		.amdhsa_next_free_sgpr 44
		.amdhsa_accum_offset 184
		.amdhsa_reserve_vcc 1
		.amdhsa_float_round_mode_32 0
		.amdhsa_float_round_mode_16_64 0
		.amdhsa_float_denorm_mode_32 3
		.amdhsa_float_denorm_mode_16_64 3
		.amdhsa_dx10_clamp 1
		.amdhsa_ieee_mode 1
		.amdhsa_fp16_overflow 0
		.amdhsa_tg_split 0
		.amdhsa_exception_fp_ieee_invalid_op 0
		.amdhsa_exception_fp_denorm_src 0
		.amdhsa_exception_fp_ieee_div_zero 0
		.amdhsa_exception_fp_ieee_overflow 0
		.amdhsa_exception_fp_ieee_underflow 0
		.amdhsa_exception_fp_ieee_inexact 0
		.amdhsa_exception_int_div_zero 0
	.end_amdhsa_kernel

.LBB4_39:
	s_waitcnt vmcnt(5)
	v_rcp_f32_e32 v2, v133
	s_waitcnt vmcnt(4)
	v_rcp_f32_e32 v3, v132
	s_waitcnt vmcnt(3)
	v_rcp_f32_e32 v4, v131
	v_cmp_lt_f32_e32 vcc, 0, v133
	s_waitcnt vmcnt(2)
	v_rcp_f32_e32 v5, v130
	s_waitcnt vmcnt(1)
	v_rcp_f32_e32 v6, v129
	v_cndmask_b32_e32 v2, 0, v2, vcc
	v_cmp_lt_f32_e32 vcc, 0, v132
	s_waitcnt vmcnt(0)
	v_rcp_f32_e32 v7, v128
	s_getpc_b64 s[36:37]
	s_sub_u32 s36, s36, 0x9238
	s_subb_u32 s37, s37, 0
	v_lshlrev_b32_e32 v183, 6, v0
	v_min_u32_e32 v183, 0x1980, v183
	global_load_dword v183, v183, s[36:37]
	v_lshlrev_b32_e32 v182, 6, v38
	global_load_dword v182, v182, s[38:39]
	s_sub_u32 s40, s36, 0x2180
	s_subb_u32 s41, s37, 0
	v_lshlrev_b32_e32 v181, 6, v38
	v_min_u32_e32 v181, 0x140, v181
	global_load_dword v181, v181, s[40:41]
	s_mov_b32 s4, 0x42c80000
	v_cndmask_b32_e32 v3, 0, v3, vcc
	v_cmp_lt_f32_e32 vcc, 0, v131
	v_cmp_ngt_f32_e64 s[2:3], s4, v3
	s_mov_b64 s[6:7], 0
	v_cndmask_b32_e32 v4, 0, v4, vcc
	v_cmp_lt_f32_e32 vcc, 0, v130
	s_nop 1
	v_cndmask_b32_e32 v5, 0, v5, vcc
	v_cmp_lt_f32_e32 vcc, 0, v129
	s_nop 1
	v_cndmask_b32_e32 v6, 0, v6, vcc
	v_cmp_lt_f32_e32 vcc, 0, v128
	s_nop 1
	v_cndmask_b32_e32 v7, 0, v7, vcc
	v_cmp_ngt_f32_e32 vcc, s4, v2
	s_or_b64 s[2:3], vcc, s[2:3]
	v_cmp_ngt_f32_e32 vcc, s4, v4
	s_or_b64 s[2:3], s[2:3], vcc
	v_cmp_ngt_f32_e32 vcc, s4, v5
	s_or_b64 s[2:3], s[2:3], vcc
	v_cmp_ngt_f32_e32 vcc, s4, v6
	s_or_b64 s[2:3], s[2:3], vcc
	v_cmp_ngt_f32_e32 vcc, s4, v7
	s_or_b64 s[2:3], s[2:3], vcc
	v_cndmask_b32_e64 v8, 0, 1, s[2:3]
	v_cmp_ne_u32_e32 vcc, 0, v8
	s_cmp_eq_u64 vcc, 0
	s_cselect_b64 s[2:3], -1, 0
	v_cndmask_b32_e64 v8, 0, 1, s[2:3]
	s_nop 0
	v_readfirstlane_b32 s2, v8
	s_bitcmp0_b32 s2, 0
	s_cbranch_scc0 .LBB4_45
	s_cmp_lt_i32 s28, 4
	s_cbranch_scc1 .LBB4_46
	s_cmp_gt_i32 s28, 4
	s_cbranch_scc0 .LBB4_47
	s_mov_b64 s[4:5], -1
	v_mov_b32_e32 v8, 0
	s_cmp_gt_i32 s28, 5
	v_mov_b32_e32 v167, 0
	v_mov_b32_e32 v166, 0
	v_mov_b32_e32 v165, 0
	v_mov_b32_e32 v164, 0
	v_mov_b32_e32 v162, 0
	v_mov_b32_e32 v160, 0
	v_mov_b32_e32 v159, 0
	v_mov_b32_e32 v157, 0
	v_mov_b32_e32 v151, 0
	v_mov_b32_e32 v149, 0
	v_mov_b32_e32 v147, 0
	v_mov_b32_e32 v146, 0
	v_mov_b32_e32 v144, 0
	v_mov_b32_e32 v143, 0
	v_mov_b32_e32 v152, 0
	v_mov_b32_e32 v153, 0
	v_mov_b32_e32 v154, 0
	v_mov_b32_e32 v155, 0
	v_mov_b32_e32 v156, 0
	v_mov_b32_e32 v158, 0
	v_mov_b32_e32 v161, 0
	v_mov_b32_e32 v163, 0
	v_mov_b32_e32 v168, 0
	v_mov_b32_e32 v169, 0
	v_mov_b32_e32 v170, 0
	v_mov_b32_e32 v171, 0
	v_mov_b32_e32 v172, 0
	v_mov_b32_e32 v173, 0
	v_mov_b32_e32 v174, 0
	v_mov_b32_e32 v145, 0
	v_mov_b32_e32 v148, 0
	v_mov_b32_e32 v150, 0
	s_cbranch_scc0 .LBB4_50
	s_cmp_eq_u32 s28, 6
	s_cbranch_scc0 .LBB4_49
	v_mov_b32_e32 v145, 0
	v_mov_b32_e32 v148, 0
	v_mov_b32_e32 v150, 0
	v_mov_b32_e32 v143, 0
	v_mov_b32_e32 v144, 0
	v_mov_b32_e32 v146, 0
	v_mov_b32_e32 v147, 0
	v_mov_b32_e32 v149, 0
	v_mov_b32_e32 v151, 0
	v_mov_b32_e32 v152, 0
	v_mov_b32_e32 v153, 0
	v_mov_b32_e32 v154, 0
	v_mov_b32_e32 v155, 0
	v_mov_b32_e32 v156, 0
	v_mov_b32_e32 v158, 0
	v_mov_b32_e32 v161, 0
	v_mov_b32_e32 v163, 0
	v_mov_b32_e32 v157, 0
	v_mov_b32_e32 v159, 0
	v_mov_b32_e32 v160, 0
	v_mov_b32_e32 v162, 0
	v_mov_b32_e32 v164, 0
	v_mov_b32_e32 v165, 0
	v_mov_b32_e32 v166, 0
	v_mov_b32_e32 v167, 0
	v_mov_b32_e32 v168, 0
	v_mov_b32_e32 v169, 0
	v_mov_b32_e32 v170, 0
	v_mov_b32_e32 v171, 0
	v_mov_b32_e32 v172, 0
	v_mov_b32_e32 v173, 0
	v_mov_b32_e32 v174, 0
	v_fma_mix_f32 v148, v43, v7, v148 op_sel_hi:[1,0,0]
	v_fma_mix_f32 v150, v45, v7, v150 op_sel_hi:[1,0,0]
	v_fma_mix_f32 v143, v50, v7, v143 op_sel_hi:[1,0,0]
	v_fma_mix_f32 v144, v54, v7, v144 op_sel_hi:[1,0,0]
	v_fma_mix_f32 v146, v58, v7, v146 op_sel_hi:[1,0,0]
	v_fma_mix_f32 v147, v61, v7, v147 op_sel_hi:[1,0,0]
	v_fma_mix_f32 v149, v64, v7, v149 op_sel_hi:[1,0,0]
	v_fma_mix_f32 v151, v66, v7, v151 op_sel_hi:[1,0,0]
	v_fma_mix_f32 v152, v43, v7, v152 op_sel:[1,0,0] op_sel_hi:[1,0,0]
	v_fma_mix_f32 v153, v45, v7, v153 op_sel:[1,0,0] op_sel_hi:[1,0,0]
	v_fma_mix_f32 v154, v50, v7, v154 op_sel:[1,0,0] op_sel_hi:[1,0,0]
	v_fma_mix_f32 v155, v54, v7, v155 op_sel:[1,0,0] op_sel_hi:[1,0,0]
	v_fma_mix_f32 v156, v58, v7, v156 op_sel:[1,0,0] op_sel_hi:[1,0,0]
	v_fma_mix_f32 v158, v61, v7, v158 op_sel:[1,0,0] op_sel_hi:[1,0,0]
	v_fma_mix_f32 v161, v64, v7, v161 op_sel:[1,0,0] op_sel_hi:[1,0,0]
	v_fma_mix_f32 v163, v66, v7, v163 op_sel:[1,0,0] op_sel_hi:[1,0,0]
	v_fma_mix_f32 v157, v72, v7, v157 op_sel_hi:[1,0,0]
	v_fma_mix_f32 v159, v76, v7, v159 op_sel_hi:[1,0,0]
	v_fma_mix_f32 v160, v83, v7, v160 op_sel_hi:[1,0,0]
	v_fma_mix_f32 v162, v85, v7, v162 op_sel_hi:[1,0,0]
	v_fma_mix_f32 v164, v89, v7, v164 op_sel_hi:[1,0,0]
	v_fma_mix_f32 v165, v92, v7, v165 op_sel_hi:[1,0,0]
	v_fma_mix_f32 v166, v95, v7, v166 op_sel_hi:[1,0,0]
	v_fma_mix_f32 v167, v96, v7, v167 op_sel_hi:[1,0,0]
	v_fma_mix_f32 v168, v72, v7, v168 op_sel:[1,0,0] op_sel_hi:[1,0,0]
	v_fma_mix_f32 v169, v76, v7, v169 op_sel:[1,0,0] op_sel_hi:[1,0,0]
	v_fma_mix_f32 v170, v83, v7, v170 op_sel:[1,0,0] op_sel_hi:[1,0,0]
	v_fma_mix_f32 v171, v85, v7, v171 op_sel:[1,0,0] op_sel_hi:[1,0,0]
	v_fma_mix_f32 v172, v89, v7, v172 op_sel:[1,0,0] op_sel_hi:[1,0,0]
	v_fma_mix_f32 v173, v92, v7, v173 op_sel:[1,0,0] op_sel_hi:[1,0,0]
	v_fma_mix_f32 v174, v95, v7, v174 op_sel:[1,0,0] op_sel_hi:[1,0,0]
	v_fma_mix_f32 v145, v96, v7, v145 op_sel:[1,0,0] op_sel_hi:[1,0,0]
	s_branch .LBB4_50

	.amdhsa_kernel _Z6k_iterILb0ELb1EEvPKfS1_PKiPK15HIP_vector_typeIfLj4EES7_S1_S1_S3_S1_PfS8_S1_S3_PDF16_PS5_SA_PiSA_SB_
		.amdhsa_group_segment_fixed_size 5808
		.amdhsa_private_segment_fixed_size 0
		.amdhsa_kernarg_size 152
		.amdhsa_user_sgpr_count 2
		.amdhsa_user_sgpr_dispatch_ptr 0
		.amdhsa_user_sgpr_queue_ptr 0
		.amdhsa_user_sgpr_kernarg_segment_ptr 1
		.amdhsa_user_sgpr_dispatch_id 0
		.amdhsa_user_sgpr_kernarg_preload_length 0
		.amdhsa_user_sgpr_kernarg_preload_offset 0
		.amdhsa_user_sgpr_private_segment_size 0
		.amdhsa_uses_dynamic_stack 0
		.amdhsa_enable_private_segment 0
		.amdhsa_system_sgpr_workgroup_id_x 1
		.amdhsa_system_sgpr_workgroup_id_y 0
		.amdhsa_system_sgpr_workgroup_id_z 0
		.amdhsa_system_sgpr_workgroup_info 0
		.amdhsa_system_vgpr_workitem_id 0
		.amdhsa_next_free_vgpr 184
		.amdhsa_next_free_sgpr 44
		.amdhsa_accum_offset 184
		.amdhsa_reserve_vcc 1
		.amdhsa_float_round_mode_32 0
		.amdhsa_float_round_mode_16_64 0
		.amdhsa_float_denorm_mode_32 3
		.amdhsa_float_denorm_mode_16_64 3
		.amdhsa_dx10_clamp 1
		.amdhsa_ieee_mode 1
		.amdhsa_fp16_overflow 0
		.amdhsa_tg_split 0
		.amdhsa_exception_fp_ieee_invalid_op 0
		.amdhsa_exception_fp_denorm_src 0
		.amdhsa_exception_fp_ieee_div_zero 0
		.amdhsa_exception_fp_ieee_overflow 0
		.amdhsa_exception_fp_ieee_underflow 0
		.amdhsa_exception_fp_ieee_inexact 0
		.amdhsa_exception_int_div_zero 0
	.end_amdhsa_kernel

amdhsa.kernels:
  - .agpr_count:     0
    .args:
      - .actual_access:  read_only
        .address_space:  global
        .offset:         0
        .size:           8
        .value_kind:     global_buffer
      - .actual_access:  read_only
        .address_space:  global
        .offset:         8
        .size:           8
        .value_kind:     global_buffer
      - .actual_access:  read_only
        .address_space:  global
        .offset:         16
        .size:           8
        .value_kind:     global_buffer
      - .actual_access:  read_only
        .address_space:  global
        .offset:         24
        .size:           8
        .value_kind:     global_buffer
      - .actual_access:  write_only
        .address_space:  global
        .offset:         32
        .size:           8
        .value_kind:     global_buffer
      - .actual_access:  write_only
        .address_space:  global
        .offset:         40
        .size:           8
        .value_kind:     global_buffer
      - .actual_access:  write_only
        .address_space:  global
        .offset:         48
        .size:           8
        .value_kind:     global_buffer
      - .actual_access:  write_only
        .address_space:  global
        .offset:         56
        .size:           8
        .value_kind:     global_buffer
      - .actual_access:  write_only
        .address_space:  global
        .offset:         64
        .size:           8
        .value_kind:     global_buffer
      - .actual_access:  write_only
        .address_space:  global
        .offset:         72
        .size:           8
        .value_kind:     global_buffer
      - .actual_access:  write_only
        .address_space:  global
        .offset:         80
        .size:           8
        .value_kind:     global_buffer
      - .actual_access:  write_only
        .address_space:  global
        .offset:         88
        .size:           8
        .value_kind:     global_buffer
      - .actual_access:  write_only
        .address_space:  global
        .offset:         96
        .size:           8
        .value_kind:     global_buffer
      - .actual_access:  write_only
        .address_space:  global
        .offset:         104
        .size:           8
        .value_kind:     global_buffer
      - .actual_access:  write_only
        .address_space:  global
        .offset:         112
        .size:           8
        .value_kind:     global_buffer
    .group_segment_fixed_size: 67584
    .kernarg_segment_align: 8
    .kernarg_segment_size: 120
    .language:       OpenCL C
    .language_version:
      - 2
      - 0
    .max_flat_workgroup_size: 1024
    .name:           _Z6k_sortPKfS0_PKiS2_PiP15HIP_vector_typeIfLj4EEPfS7_S3_S7_S7_S3_S3_S6_S6_
    .private_segment_fixed_size: 0
    .sgpr_count:     58
    .sgpr_spill_count: 0
    .symbol:         _Z6k_sortPKfS0_PKiS2_PiP15HIP_vector_typeIfLj4EEPfS7_S3_S7_S7_S3_S3_S6_S6_.kd
    .uniform_work_group_size: 1
    .uses_dynamic_stack: false
    .vgpr_count:     48
    .vgpr_spill_count: 0
    .wavefront_size: 64
  - .agpr_count:     0
    .args:
      - .actual_access:  read_only
        .address_space:  global
        .offset:         0
        .size:           8
        .value_kind:     global_buffer
      - .actual_access:  read_only
        .address_space:  global
        .offset:         8
        .size:           8
        .value_kind:     global_buffer
      - .actual_access:  read_only
        .address_space:  global
        .offset:         16
        .size:           8
        .value_kind:     global_buffer
      - .actual_access:  read_only
        .address_space:  global
        .offset:         24
        .size:           8
        .value_kind:     global_buffer
      - .actual_access:  read_only
        .address_space:  global
        .offset:         32
        .size:           8
        .value_kind:     global_buffer
      - .actual_access:  read_only
        .address_space:  global
        .offset:         40
        .size:           8
        .value_kind:     global_buffer
      - .actual_access:  read_only
        .address_space:  global
        .offset:         48
        .size:           8
        .value_kind:     global_buffer
      - .actual_access:  write_only
        .address_space:  global
        .offset:         56
        .size:           8
        .value_kind:     global_buffer
    .group_segment_fixed_size: 145952
    .kernarg_segment_align: 8
    .kernarg_segment_size: 64
    .language:       OpenCL C
    .language_version:
      - 2
      - 0
    .max_flat_workgroup_size: 512
    .name:           _Z7k_finalPK15HIP_vector_typeIfLj4EES2_PKiS4_PKfS6_PKDF16_Pf
    .private_segment_fixed_size: 0
    .sgpr_count:     34
    .sgpr_spill_count: 0
    .symbol:         _Z7k_finalPK15HIP_vector_typeIfLj4EES2_PKiS4_PKfS6_PKDF16_Pf.kd
    .uniform_work_group_size: 1
    .uses_dynamic_stack: false
    .vgpr_count:     177
    .vgpr_spill_count: 0
    .wavefront_size: 64
  - .agpr_count:     0
    .args:
      - .actual_access:  read_only
        .address_space:  global
        .offset:         0
        .size:           8
        .value_kind:     global_buffer
      - .actual_access:  read_only
        .address_space:  global
        .offset:         8
        .size:           8
        .value_kind:     global_buffer
      - .actual_access:  read_only
        .address_space:  global
        .offset:         16
        .size:           8
        .value_kind:     global_buffer
      - .actual_access:  read_only
        .address_space:  global
        .offset:         24
        .size:           8
        .value_kind:     global_buffer
      - .actual_access:  read_only
        .address_space:  global
        .offset:         32
        .size:           8
        .value_kind:     global_buffer
      - .actual_access:  read_only
        .address_space:  global
        .offset:         40
        .size:           8
        .value_kind:     global_buffer
      - .actual_access:  read_only
        .address_space:  global
        .offset:         48
        .size:           8
        .value_kind:     global_buffer
      - .actual_access:  read_only
        .address_space:  global
        .offset:         56
        .size:           8
        .value_kind:     global_buffer
      - .actual_access:  read_only
        .address_space:  global
        .offset:         64
        .size:           8
        .value_kind:     global_buffer
      - .address_space:  global
        .offset:         72
        .size:           8
        .value_kind:     global_buffer
      - .actual_access:  read_only
        .address_space:  global
        .offset:         80
        .size:           8
        .value_kind:     global_buffer
      - .actual_access:  read_only
        .address_space:  global
        .offset:         88
        .size:           8
        .value_kind:     global_buffer
      - .actual_access:  read_only
        .address_space:  global
        .offset:         96
        .size:           8
        .value_kind:     global_buffer
      - .actual_access:  write_only
        .address_space:  global
        .offset:         104
        .size:           8
        .value_kind:     global_buffer
      - .address_space:  global
        .offset:         112
        .size:           8
        .value_kind:     global_buffer
      - .actual_access:  write_only
        .address_space:  global
        .offset:         120
        .size:           8
        .value_kind:     global_buffer
      - .actual_access:  write_only
        .address_space:  global
        .offset:         128
        .size:           8
        .value_kind:     global_buffer
      - .actual_access:  write_only
        .address_space:  global
        .offset:         136
        .size:           8
        .value_kind:     global_buffer
      - .actual_access:  write_only
        .address_space:  global
        .offset:         144
        .size:           8
        .value_kind:     global_buffer
    .group_segment_fixed_size: 30384
    .kernarg_segment_align: 8
    .kernarg_segment_size: 152
    .language:       OpenCL C
    .language_version:
      - 2
      - 0
    .max_flat_workgroup_size: 512
    .name:           _Z6k_iterILb1ELb0EEvPKfS1_PKiPK15HIP_vector_typeIfLj4EES7_S1_S1_S3_S1_PfS8_S1_S3_PDF16_PS5_SA_PiSA_SB_
    .private_segment_fixed_size: 0
    .sgpr_count:     108
    .sgpr_spill_count: 0
    .symbol:         _Z6k_iterILb1ELb0EEvPKfS1_PKiPK15HIP_vector_typeIfLj4EES7_S1_S1_S3_S1_PfS8_S1_S3_PDF16_PS5_SA_PiSA_SB_.kd
    .uniform_work_group_size: 1
    .uses_dynamic_stack: false
    .vgpr_count:     256
    .vgpr_spill_count: 0
    .wavefront_size: 64
  - .agpr_count:     0
    .args:
      - .actual_access:  read_only
        .address_space:  global
        .offset:         0
        .size:           8
        .value_kind:     global_buffer
      - .actual_access:  read_only
        .address_space:  global
        .offset:         8
        .size:           8
        .value_kind:     global_buffer
      - .actual_access:  read_only
        .address_space:  global
        .offset:         16
        .size:           8
        .value_kind:     global_buffer
      - .actual_access:  read_only
        .address_space:  global
        .offset:         24
        .size:           8
        .value_kind:     global_buffer
      - .actual_access:  read_only
        .address_space:  global
        .offset:         32
        .size:           8
        .value_kind:     global_buffer
      - .actual_access:  read_only
        .address_space:  global
        .offset:         40
        .size:           8
        .value_kind:     global_buffer
      - .actual_access:  read_only
        .address_space:  global
        .offset:         48
        .size:           8
        .value_kind:     global_buffer
      - .actual_access:  read_only
        .address_space:  global
        .offset:         56
        .size:           8
        .value_kind:     global_buffer
      - .actual_access:  read_only
        .address_space:  global
        .offset:         64
        .size:           8
        .value_kind:     global_buffer
      - .address_space:  global
        .offset:         72
        .size:           8
        .value_kind:     global_buffer
      - .actual_access:  read_only
        .address_space:  global
        .offset:         80
        .size:           8
        .value_kind:     global_buffer
      - .actual_access:  read_only
        .address_space:  global
        .offset:         88
        .size:           8
        .value_kind:     global_buffer
      - .actual_access:  read_only
        .address_space:  global
        .offset:         96
        .size:           8
        .value_kind:     global_buffer
      - .actual_access:  read_only
        .address_space:  global
        .offset:         104
        .size:           8
        .value_kind:     global_buffer
      - .actual_access:  read_only
        .address_space:  global
        .offset:         112
        .size:           8
        .value_kind:     global_buffer
      - .actual_access:  read_only
        .address_space:  global
        .offset:         120
        .size:           8
        .value_kind:     global_buffer
      - .actual_access:  read_only
        .address_space:  global
        .offset:         128
        .size:           8
        .value_kind:     global_buffer
      - .actual_access:  read_only
        .address_space:  global
        .offset:         136
        .size:           8
        .value_kind:     global_buffer
      - .actual_access:  read_only
        .address_space:  global
        .offset:         144
        .size:           8
        .value_kind:     global_buffer
    .group_segment_fixed_size: 5808
    .kernarg_segment_align: 8
    .kernarg_segment_size: 152
    .language:       OpenCL C
    .language_version:
      - 2
      - 0
    .max_flat_workgroup_size: 512
    .name:           _Z6k_iterILb0ELb0EEvPKfS1_PKiPK15HIP_vector_typeIfLj4EES7_S1_S1_S3_S1_PfS8_S1_S3_PDF16_PS5_SA_PiSA_SB_
    .private_segment_fixed_size: 0
    .sgpr_count:     50
    .sgpr_spill_count: 0
    .symbol:         _Z6k_iterILb0ELb0EEvPKfS1_PKiPK15HIP_vector_typeIfLj4EES7_S1_S1_S3_S1_PfS8_S1_S3_PDF16_PS5_SA_PiSA_SB_.kd
    .uniform_work_group_size: 1
    .uses_dynamic_stack: false
    .vgpr_count:     184
    .vgpr_spill_count: 0
    .wavefront_size: 64
  - .agpr_count:     0
    .args:
      - .actual_access:  read_only
        .address_space:  global
        .offset:         0
        .size:           8
        .value_kind:     global_buffer
      - .actual_access:  read_only
        .address_space:  global
        .offset:         8
        .size:           8
        .value_kind:     global_buffer
      - .actual_access:  read_only
        .address_space:  global
        .offset:         16
        .size:           8
        .value_kind:     global_buffer
      - .actual_access:  read_only
        .address_space:  global
        .offset:         24
        .size:           8
        .value_kind:     global_buffer
      - .actual_access:  read_only
        .address_space:  global
        .offset:         32
        .size:           8
        .value_kind:     global_buffer
      - .actual_access:  read_only
        .address_space:  global
        .offset:         40
        .size:           8
        .value_kind:     global_buffer
      - .actual_access:  read_only
        .address_space:  global
        .offset:         48
        .size:           8
        .value_kind:     global_buffer
      - .actual_access:  read_only
        .address_space:  global
        .offset:         56
        .size:           8
        .value_kind:     global_buffer
      - .actual_access:  read_only
        .address_space:  global
        .offset:         64
        .size:           8
        .value_kind:     global_buffer
      - .address_space:  global
        .offset:         72
        .size:           8
        .value_kind:     global_buffer
      - .actual_access:  write_only
        .address_space:  global
        .offset:         80
        .size:           8
        .value_kind:     global_buffer
      - .actual_access:  read_only
        .address_space:  global
        .offset:         88
        .size:           8
        .value_kind:     global_buffer
      - .actual_access:  read_only
        .address_space:  global
        .offset:         96
        .size:           8
        .value_kind:     global_buffer
      - .actual_access:  read_only
        .address_space:  global
        .offset:         104
        .size:           8
        .value_kind:     global_buffer
      - .actual_access:  read_only
        .address_space:  global
        .offset:         112
        .size:           8
        .value_kind:     global_buffer
      - .actual_access:  read_only
        .address_space:  global
        .offset:         120
        .size:           8
        .value_kind:     global_buffer
      - .actual_access:  read_only
        .address_space:  global
        .offset:         128
        .size:           8
        .value_kind:     global_buffer
      - .actual_access:  read_only
        .address_space:  global
        .offset:         136
        .size:           8
        .value_kind:     global_buffer
      - .actual_access:  read_only
        .address_space:  global
        .offset:         144
        .size:           8
        .value_kind:     global_buffer
    .group_segment_fixed_size: 5808
    .kernarg_segment_align: 8
    .kernarg_segment_size: 152
    .language:       OpenCL C
    .language_version:
      - 2
      - 0
    .max_flat_workgroup_size: 512
    .name:           _Z6k_iterILb0ELb1EEvPKfS1_PKiPK15HIP_vector_typeIfLj4EES7_S1_S1_S3_S1_PfS8_S1_S3_PDF16_PS5_SA_PiSA_SB_
    .private_segment_fixed_size: 0
    .sgpr_count:     50
    .sgpr_spill_count: 0
    .symbol:         _Z6k_iterILb0ELb1EEvPKfS1_PKiPK15HIP_vector_typeIfLj4EES7_S1_S1_S3_S1_PfS8_S1_S3_PDF16_PS5_SA_PiSA_SB_.kd
    .uniform_work_group_size: 1
    .uses_dynamic_stack: false
    .vgpr_count:     184
    .vgpr_spill_count: 0
    .wavefront_size: 64
